# P8 gate_up set-up: 42 serialized table loads (each behind vmcnt(0)) issued together, one wait, deferred post-ops
# speedup vs baseline: 1.0133x; 1.0001x over previous
; __device__ __forceinline__ unsigned f2bf(float f) { return pk2(f, 0.f) & 0xffffu; }
; __global__ void __launch_bounds__(NTHREADS, 2) fwd(Args args) {
;     ...
;             { int pr[EPT_RL]; float pv[EPT_RL]; const int t8 = tid & 255;
; #pragma unroll
;               for (int i = 0; i < EPT_RL; ++i) { pg8::Unit pu; const bool ok = S.next(i, pu); pr[i] = (ok && t8 < pu.nv) ? LIST[pu.e * T + pu.mt * 256 + t8] >> 2 : 0;
;                   pv[i] = ok ? b_gu[(size_t)pu.e * 4096 + (t8 >> 7) * 2048 + pu.pn * 128 + (t8 & 127)] : 0.f; }
; #pragma unroll
;               for (int i = 0; i < EPT_RL; ++i) if (tid < 256) { RL[i * 256 + tid] = (unsigned short)pr[i]; BT[i * 256 + tid] = (bf16)f2bf(pv[i]); } }
.LBB0_891:
.LBB0_892:
	v_cmp_lt_i32_sdwa s[10:11], v0, s2 src0_sel:BYTE_0 src1_sel:DWORD
	s_and_b64 s[14:15], s[8:9], s[10:11]
	v_mov_b32_e32 v3, 0
	v_mov_b32_e32 v9, 0
	s_and_saveexec_b64 s[10:11], s[14:15]
	s_cbranch_execz .LBB0_894
	s_lshl_b32 s5, s4, 14
	s_lshl_b32 s13, s12, 8
	s_add_i32 s5, s5, s13
	v_or_b32_sdwa v4, s5, v0 dst_sel:DWORD dst_unused:UNUSED_PAD src0_sel:DWORD src1_sel:BYTE_0
	v_ashrrev_i32_e32 v5, 31, v4
	v_lshl_add_u64 v[4:5], v[4:5], 2, s[24:25]
	global_load_dword v9, v[4:5], off
.LBB0_894:
	s_or_b64 exec, exec, s[10:11]
	v_lshlrev_b32_e32 v8, 6, v0
	v_readlane_b32 s36, v246, 0
	v_and_b32_e32 v4, 0x7f, v0
	v_and_b32_e32 v2, 0x2000, v8
	v_readlane_b32 s37, v246, 1
	s_andn2_b64 vcc, exec, s[8:9]
	v_lshlrev_b32_e32 v4, 2, v4
	v_lshl_add_u64 v[6:7], s[36:37], 0, v[2:3]
	v_readlane_b32 s38, v246, 2
	v_readlane_b32 s39, v246, 3
	v_readlane_b32 s40, v246, 4
	v_readlane_b32 s41, v246, 5
	v_readlane_b32 s42, v246, 6
	v_readlane_b32 s43, v246, 7
	s_cbranch_vccnz .LBB0_896
	s_ashr_i32 s5, s4, 31
	s_lshl_b32 s8, s3, 7
	s_lshl_b64 s[10:11], s[4:5], 14
	s_ashr_i32 s9, s8, 31
	v_lshl_add_u64 v[2:3], v[6:7], 0, s[10:11]
	v_lshl_add_u64 v[2:3], s[8:9], 2, v[2:3]
	v_mov_b32_e32 v5, 0
	v_lshl_add_u64 v[2:3], v[2:3], 0, v[4:5]
	global_load_dword v3, v[2:3], off

; __global__ void __launch_bounds__(NTHREADS, 2) fwd(Args args) {
;     ...
;             { int pr[EPT_RL]; float pv[EPT_RL]; const int t8 = tid & 255;
; #pragma unroll
;               for (int i = 0; i < EPT_RL; ++i) { pg8::Unit pu; const bool ok = S.next(i, pu); pr[i] = (ok && t8 < pu.nv) ? LIST[pu.e * T + pu.mt * 256 + t8] >> 2 : 0;
;                   pv[i] = ok ? b_gu[(size_t)pu.e * 4096 + (t8 >> 7) * 2048 + pu.pn * 128 + (t8 & 127)] : 0.f; }
.LBB0_900:
	s_or_b64 exec, exec, s[10:11]
	s_andn2_b64 vcc, exec, s[8:9]
	s_cbranch_vccnz .LBB0_902
	s_ashr_i32 s5, s4, 31
	s_lshl_b32 s8, s3, 7
	s_lshl_b64 s[10:11], s[4:5], 14
	s_ashr_i32 s9, s8, 31
	v_lshl_add_u64 v[10:11], v[6:7], 0, s[10:11]
	v_lshl_add_u64 v[10:11], s[8:9], 2, v[10:11]
	v_mov_b32_e32 v5, 0
	v_lshl_add_u64 v[10:11], v[10:11], 0, v[4:5]
	global_load_dword v10, v[10:11], off

; __global__ void __launch_bounds__(NTHREADS, 2) fwd(Args args) {
;     ...
;             { int pr[EPT_RL]; float pv[EPT_RL]; const int t8 = tid & 255;
; #pragma unroll
;               for (int i = 0; i < EPT_RL; ++i) { pg8::Unit pu; const bool ok = S.next(i, pu); pr[i] = (ok && t8 < pu.nv) ? LIST[pu.e * T + pu.mt * 256 + t8] >> 2 : 0;
;                   pv[i] = ok ? b_gu[(size_t)pu.e * 4096 + (t8 >> 7) * 2048 + pu.pn * 128 + (t8 & 127)] : 0.f; }
.LBB0_904:
	v_cmp_lt_i32_sdwa s[10:11], v0, s2 src0_sel:BYTE_0 src1_sel:DWORD
	s_and_b64 s[14:15], s[8:9], s[10:11]
	v_mov_b32_e32 v12, 0
	v_mov_b32_e32 v11, 0
	s_and_saveexec_b64 s[10:11], s[14:15]
	s_cbranch_execz .LBB0_906
	s_lshl_b32 s5, s4, 14
	s_lshl_b32 s13, s12, 8
	s_add_i32 s5, s5, s13
	v_or_b32_sdwa v14, s5, v0 dst_sel:DWORD dst_unused:UNUSED_PAD src0_sel:DWORD src1_sel:BYTE_0
	v_ashrrev_i32_e32 v15, 31, v14
	v_lshl_add_u64 v[14:15], v[14:15], 2, s[24:25]
	global_load_dword v11, v[14:15], off
.LBB0_906:
	s_or_b64 exec, exec, s[10:11]
	s_andn2_b64 vcc, exec, s[8:9]
	s_cbranch_vccnz .LBB0_908
	s_ashr_i32 s5, s4, 31
	s_lshl_b32 s8, s3, 7
	s_lshl_b64 s[10:11], s[4:5], 14
	s_ashr_i32 s9, s8, 31
	v_lshl_add_u64 v[12:13], v[6:7], 0, s[10:11]
	v_lshl_add_u64 v[12:13], s[8:9], 2, v[12:13]
	v_mov_b32_e32 v5, 0
	v_lshl_add_u64 v[12:13], v[12:13], 0, v[4:5]
	global_load_dword v12, v[12:13], off

; __global__ void __launch_bounds__(NTHREADS, 2) fwd(Args args) {
;     ...
;             { int pr[EPT_RL]; float pv[EPT_RL]; const int t8 = tid & 255;
; #pragma unroll
;               for (int i = 0; i < EPT_RL; ++i) { pg8::Unit pu; const bool ok = S.next(i, pu); pr[i] = (ok && t8 < pu.nv) ? LIST[pu.e * T + pu.mt * 256 + t8] >> 2 : 0;
;                   pv[i] = ok ? b_gu[(size_t)pu.e * 4096 + (t8 >> 7) * 2048 + pu.pn * 128 + (t8 & 127)] : 0.f; }
.LBB0_910:
	v_cmp_lt_i32_sdwa s[10:11], v0, s2 src0_sel:BYTE_0 src1_sel:DWORD
	s_and_b64 s[14:15], s[8:9], s[10:11]
	v_mov_b32_e32 v14, 0
	v_mov_b32_e32 v13, 0
	s_and_saveexec_b64 s[10:11], s[14:15]
	s_cbranch_execz .LBB0_912
	s_lshl_b32 s5, s4, 14
	s_lshl_b32 s13, s12, 8
	s_add_i32 s5, s5, s13
	v_or_b32_sdwa v16, s5, v0 dst_sel:DWORD dst_unused:UNUSED_PAD src0_sel:DWORD src1_sel:BYTE_0
	v_ashrrev_i32_e32 v17, 31, v16
	v_lshl_add_u64 v[16:17], v[16:17], 2, s[24:25]
	global_load_dword v13, v[16:17], off
.LBB0_912:
	s_or_b64 exec, exec, s[10:11]
	s_andn2_b64 vcc, exec, s[8:9]
	s_cbranch_vccnz .LBB0_914
	s_ashr_i32 s5, s4, 31
	s_lshl_b32 s8, s3, 7
	s_lshl_b64 s[10:11], s[4:5], 14
	s_ashr_i32 s9, s8, 31
	v_lshl_add_u64 v[14:15], v[6:7], 0, s[10:11]
	v_lshl_add_u64 v[14:15], s[8:9], 2, v[14:15]
	v_mov_b32_e32 v5, 0
	v_lshl_add_u64 v[14:15], v[14:15], 0, v[4:5]
	global_load_dword v14, v[14:15], off

; __global__ void __launch_bounds__(NTHREADS, 2) fwd(Args args) {
;     ...
;             { int pr[EPT_RL]; float pv[EPT_RL]; const int t8 = tid & 255;
; #pragma unroll
;               for (int i = 0; i < EPT_RL; ++i) { pg8::Unit pu; const bool ok = S.next(i, pu); pr[i] = (ok && t8 < pu.nv) ? LIST[pu.e * T + pu.mt * 256 + t8] >> 2 : 0;
;                   pv[i] = ok ? b_gu[(size_t)pu.e * 4096 + (t8 >> 7) * 2048 + pu.pn * 128 + (t8 & 127)] : 0.f; }
.LBB0_916:
	v_cmp_lt_i32_sdwa s[10:11], v0, s2 src0_sel:BYTE_0 src1_sel:DWORD
	s_and_b64 s[14:15], s[8:9], s[10:11]
	v_mov_b32_e32 v16, 0
	v_mov_b32_e32 v15, 0
	s_and_saveexec_b64 s[10:11], s[14:15]
	s_cbranch_execz .LBB0_918
	s_lshl_b32 s5, s4, 14
	s_lshl_b32 s13, s12, 8
	s_add_i32 s5, s5, s13
	v_or_b32_sdwa v18, s5, v0 dst_sel:DWORD dst_unused:UNUSED_PAD src0_sel:DWORD src1_sel:BYTE_0
	v_ashrrev_i32_e32 v19, 31, v18
	v_lshl_add_u64 v[18:19], v[18:19], 2, s[24:25]
	global_load_dword v15, v[18:19], off
.LBB0_918:
	s_or_b64 exec, exec, s[10:11]
	s_andn2_b64 vcc, exec, s[8:9]
	s_cbranch_vccnz .LBB0_920
	s_ashr_i32 s5, s4, 31
	s_lshl_b32 s8, s3, 7
	s_lshl_b64 s[10:11], s[4:5], 14
	s_ashr_i32 s9, s8, 31
	v_lshl_add_u64 v[16:17], v[6:7], 0, s[10:11]
	v_lshl_add_u64 v[16:17], s[8:9], 2, v[16:17]
	v_mov_b32_e32 v5, 0
	v_lshl_add_u64 v[16:17], v[16:17], 0, v[4:5]
	global_load_dword v16, v[16:17], off

; __global__ void __launch_bounds__(NTHREADS, 2) fwd(Args args) {
;     ...
;             { int pr[EPT_RL]; float pv[EPT_RL]; const int t8 = tid & 255;
; #pragma unroll
;               for (int i = 0; i < EPT_RL; ++i) { pg8::Unit pu; const bool ok = S.next(i, pu); pr[i] = (ok && t8 < pu.nv) ? LIST[pu.e * T + pu.mt * 256 + t8] >> 2 : 0;
;                   pv[i] = ok ? b_gu[(size_t)pu.e * 4096 + (t8 >> 7) * 2048 + pu.pn * 128 + (t8 & 127)] : 0.f; }
.LBB0_922:
	v_cmp_lt_i32_sdwa s[10:11], v0, s2 src0_sel:BYTE_0 src1_sel:DWORD
	s_and_b64 s[14:15], s[8:9], s[10:11]
	v_mov_b32_e32 v18, 0
	v_mov_b32_e32 v17, 0
	s_and_saveexec_b64 s[10:11], s[14:15]
	s_cbranch_execz .LBB0_924
	s_lshl_b32 s5, s4, 14
	s_lshl_b32 s13, s12, 8
	s_add_i32 s5, s5, s13
	v_or_b32_sdwa v20, s5, v0 dst_sel:DWORD dst_unused:UNUSED_PAD src0_sel:DWORD src1_sel:BYTE_0
	v_ashrrev_i32_e32 v21, 31, v20
	v_lshl_add_u64 v[20:21], v[20:21], 2, s[24:25]
	global_load_dword v17, v[20:21], off
.LBB0_924:
	s_or_b64 exec, exec, s[10:11]
	s_andn2_b64 vcc, exec, s[8:9]
	s_cbranch_vccnz .LBB0_926
	s_ashr_i32 s5, s4, 31
	s_lshl_b32 s8, s3, 7
	s_lshl_b64 s[10:11], s[4:5], 14
	s_ashr_i32 s9, s8, 31
	v_lshl_add_u64 v[18:19], v[6:7], 0, s[10:11]
	v_lshl_add_u64 v[18:19], s[8:9], 2, v[18:19]
	v_mov_b32_e32 v5, 0
	v_lshl_add_u64 v[18:19], v[18:19], 0, v[4:5]
	global_load_dword v18, v[18:19], off

; __global__ void __launch_bounds__(NTHREADS, 2) fwd(Args args) {
;     ...
;             { int pr[EPT_RL]; float pv[EPT_RL]; const int t8 = tid & 255;
; #pragma unroll
;               for (int i = 0; i < EPT_RL; ++i) { pg8::Unit pu; const bool ok = S.next(i, pu); pr[i] = (ok && t8 < pu.nv) ? LIST[pu.e * T + pu.mt * 256 + t8] >> 2 : 0;
;                   pv[i] = ok ? b_gu[(size_t)pu.e * 4096 + (t8 >> 7) * 2048 + pu.pn * 128 + (t8 & 127)] : 0.f; }
.LBB0_928:
	v_cmp_lt_i32_sdwa s[10:11], v0, s2 src0_sel:BYTE_0 src1_sel:DWORD
	s_and_b64 s[14:15], s[8:9], s[10:11]
	v_mov_b32_e32 v20, 0
	v_mov_b32_e32 v19, 0
	s_and_saveexec_b64 s[10:11], s[14:15]
	s_cbranch_execz .LBB0_930
	s_lshl_b32 s5, s4, 14
	s_lshl_b32 s13, s12, 8
	s_add_i32 s5, s5, s13
	v_or_b32_sdwa v22, s5, v0 dst_sel:DWORD dst_unused:UNUSED_PAD src0_sel:DWORD src1_sel:BYTE_0
	v_ashrrev_i32_e32 v23, 31, v22
	v_lshl_add_u64 v[22:23], v[22:23], 2, s[24:25]
	global_load_dword v19, v[22:23], off
.LBB0_930:
	s_or_b64 exec, exec, s[10:11]
	s_andn2_b64 vcc, exec, s[8:9]
	s_cbranch_vccnz .LBB0_932
	s_ashr_i32 s5, s4, 31
	s_lshl_b32 s8, s3, 7
	s_lshl_b64 s[10:11], s[4:5], 14
	s_ashr_i32 s9, s8, 31
	v_lshl_add_u64 v[20:21], v[6:7], 0, s[10:11]
	v_lshl_add_u64 v[20:21], s[8:9], 2, v[20:21]
	v_mov_b32_e32 v5, 0
	v_lshl_add_u64 v[20:21], v[20:21], 0, v[4:5]
	global_load_dword v20, v[20:21], off

; __global__ void __launch_bounds__(NTHREADS, 2) fwd(Args args) {
;     ...
;             { int pr[EPT_RL]; float pv[EPT_RL]; const int t8 = tid & 255;
; #pragma unroll
;               for (int i = 0; i < EPT_RL; ++i) { pg8::Unit pu; const bool ok = S.next(i, pu); pr[i] = (ok && t8 < pu.nv) ? LIST[pu.e * T + pu.mt * 256 + t8] >> 2 : 0;
;                   pv[i] = ok ? b_gu[(size_t)pu.e * 4096 + (t8 >> 7) * 2048 + pu.pn * 128 + (t8 & 127)] : 0.f; }
.LBB0_934:
	v_cmp_lt_i32_sdwa s[10:11], v0, s2 src0_sel:BYTE_0 src1_sel:DWORD
	s_and_b64 s[14:15], s[8:9], s[10:11]
	v_mov_b32_e32 v22, 0
	v_mov_b32_e32 v21, 0
	s_and_saveexec_b64 s[10:11], s[14:15]
	s_cbranch_execz .LBB0_936
	s_lshl_b32 s5, s4, 14
	s_lshl_b32 s13, s12, 8
	s_add_i32 s5, s5, s13
	v_or_b32_sdwa v24, s5, v0 dst_sel:DWORD dst_unused:UNUSED_PAD src0_sel:DWORD src1_sel:BYTE_0
	v_ashrrev_i32_e32 v25, 31, v24
	v_lshl_add_u64 v[24:25], v[24:25], 2, s[24:25]
	global_load_dword v21, v[24:25], off
.LBB0_936:
	s_or_b64 exec, exec, s[10:11]
	s_andn2_b64 vcc, exec, s[8:9]
	s_cbranch_vccnz .LBB0_938
	s_ashr_i32 s5, s4, 31
	s_lshl_b32 s8, s3, 7
	s_lshl_b64 s[10:11], s[4:5], 14
	s_ashr_i32 s9, s8, 31
	v_lshl_add_u64 v[22:23], v[6:7], 0, s[10:11]
	v_lshl_add_u64 v[22:23], s[8:9], 2, v[22:23]
	v_mov_b32_e32 v5, 0
	v_lshl_add_u64 v[22:23], v[22:23], 0, v[4:5]
	global_load_dword v22, v[22:23], off

; __global__ void __launch_bounds__(NTHREADS, 2) fwd(Args args) {
;     ...
;             { int pr[EPT_RL]; float pv[EPT_RL]; const int t8 = tid & 255;
; #pragma unroll
;               for (int i = 0; i < EPT_RL; ++i) { pg8::Unit pu; const bool ok = S.next(i, pu); pr[i] = (ok && t8 < pu.nv) ? LIST[pu.e * T + pu.mt * 256 + t8] >> 2 : 0;
;                   pv[i] = ok ? b_gu[(size_t)pu.e * 4096 + (t8 >> 7) * 2048 + pu.pn * 128 + (t8 & 127)] : 0.f; }
.LBB0_940:
	v_cmp_lt_i32_sdwa s[10:11], v0, s2 src0_sel:BYTE_0 src1_sel:DWORD
	s_and_b64 s[14:15], s[8:9], s[10:11]
	v_mov_b32_e32 v24, 0
	v_mov_b32_e32 v23, 0
	s_and_saveexec_b64 s[10:11], s[14:15]
	s_cbranch_execz .LBB0_942
	s_lshl_b32 s5, s4, 14
	s_lshl_b32 s13, s12, 8
	s_add_i32 s5, s5, s13
	v_or_b32_sdwa v26, s5, v0 dst_sel:DWORD dst_unused:UNUSED_PAD src0_sel:DWORD src1_sel:BYTE_0
	v_ashrrev_i32_e32 v27, 31, v26
	v_lshl_add_u64 v[26:27], v[26:27], 2, s[24:25]
	global_load_dword v23, v[26:27], off
.LBB0_942:
	s_or_b64 exec, exec, s[10:11]
	s_andn2_b64 vcc, exec, s[8:9]
	s_cbranch_vccnz .LBB0_944
	s_ashr_i32 s5, s4, 31
	s_lshl_b32 s8, s3, 7
	s_lshl_b64 s[10:11], s[4:5], 14
	s_ashr_i32 s9, s8, 31
	v_lshl_add_u64 v[24:25], v[6:7], 0, s[10:11]
	v_lshl_add_u64 v[24:25], s[8:9], 2, v[24:25]
	v_mov_b32_e32 v5, 0
	v_lshl_add_u64 v[24:25], v[24:25], 0, v[4:5]
	global_load_dword v24, v[24:25], off

; __global__ void __launch_bounds__(NTHREADS, 2) fwd(Args args) {
;     ...
;             { int pr[EPT_RL]; float pv[EPT_RL]; const int t8 = tid & 255;
; #pragma unroll
;               for (int i = 0; i < EPT_RL; ++i) { pg8::Unit pu; const bool ok = S.next(i, pu); pr[i] = (ok && t8 < pu.nv) ? LIST[pu.e * T + pu.mt * 256 + t8] >> 2 : 0;
;                   pv[i] = ok ? b_gu[(size_t)pu.e * 4096 + (t8 >> 7) * 2048 + pu.pn * 128 + (t8 & 127)] : 0.f; }
.LBB0_946:
	v_cmp_lt_i32_sdwa s[10:11], v0, s2 src0_sel:BYTE_0 src1_sel:DWORD
	s_and_b64 s[14:15], s[8:9], s[10:11]
	v_mov_b32_e32 v26, 0
	v_mov_b32_e32 v25, 0
	s_and_saveexec_b64 s[10:11], s[14:15]
	s_cbranch_execz .LBB0_948
	s_lshl_b32 s5, s4, 14
	s_lshl_b32 s13, s12, 8
	s_add_i32 s5, s5, s13
	v_or_b32_sdwa v28, s5, v0 dst_sel:DWORD dst_unused:UNUSED_PAD src0_sel:DWORD src1_sel:BYTE_0
	v_ashrrev_i32_e32 v29, 31, v28
	v_lshl_add_u64 v[28:29], v[28:29], 2, s[24:25]
	global_load_dword v25, v[28:29], off
.LBB0_948:
	s_or_b64 exec, exec, s[10:11]
	s_andn2_b64 vcc, exec, s[8:9]
	s_cbranch_vccnz .LBB0_950
	s_ashr_i32 s5, s4, 31
	s_lshl_b32 s8, s3, 7
	s_lshl_b64 s[10:11], s[4:5], 14
	s_ashr_i32 s9, s8, 31
	v_lshl_add_u64 v[26:27], v[6:7], 0, s[10:11]
	v_lshl_add_u64 v[26:27], s[8:9], 2, v[26:27]
	v_mov_b32_e32 v5, 0
	v_lshl_add_u64 v[26:27], v[26:27], 0, v[4:5]
	global_load_dword v26, v[26:27], off

; __global__ void __launch_bounds__(NTHREADS, 2) fwd(Args args) {
;     ...
;             { int pr[EPT_RL]; float pv[EPT_RL]; const int t8 = tid & 255;
; #pragma unroll
;               for (int i = 0; i < EPT_RL; ++i) { pg8::Unit pu; const bool ok = S.next(i, pu); pr[i] = (ok && t8 < pu.nv) ? LIST[pu.e * T + pu.mt * 256 + t8] >> 2 : 0;
;                   pv[i] = ok ? b_gu[(size_t)pu.e * 4096 + (t8 >> 7) * 2048 + pu.pn * 128 + (t8 & 127)] : 0.f; }
.LBB0_952:
	v_cmp_lt_i32_sdwa s[10:11], v0, s2 src0_sel:BYTE_0 src1_sel:DWORD
	s_and_b64 s[14:15], s[8:9], s[10:11]
	v_mov_b32_e32 v28, 0
	v_mov_b32_e32 v27, 0
	s_and_saveexec_b64 s[10:11], s[14:15]
	s_cbranch_execz .LBB0_954
	s_lshl_b32 s5, s4, 14
	s_lshl_b32 s13, s12, 8
	s_add_i32 s5, s5, s13
	v_or_b32_sdwa v30, s5, v0 dst_sel:DWORD dst_unused:UNUSED_PAD src0_sel:DWORD src1_sel:BYTE_0
	v_ashrrev_i32_e32 v31, 31, v30
	v_lshl_add_u64 v[30:31], v[30:31], 2, s[24:25]
	global_load_dword v27, v[30:31], off
.LBB0_954:
	s_or_b64 exec, exec, s[10:11]
	s_andn2_b64 vcc, exec, s[8:9]
	s_cbranch_vccnz .LBB0_956
	s_ashr_i32 s5, s4, 31
	s_lshl_b32 s8, s3, 7
	s_lshl_b64 s[10:11], s[4:5], 14
	s_ashr_i32 s9, s8, 31
	v_lshl_add_u64 v[28:29], v[6:7], 0, s[10:11]
	v_lshl_add_u64 v[28:29], s[8:9], 2, v[28:29]
	v_mov_b32_e32 v5, 0
	v_lshl_add_u64 v[28:29], v[28:29], 0, v[4:5]
	global_load_dword v28, v[28:29], off

; __global__ void __launch_bounds__(NTHREADS, 2) fwd(Args args) {
;     ...
;             { int pr[EPT_RL]; float pv[EPT_RL]; const int t8 = tid & 255;
; #pragma unroll
;               for (int i = 0; i < EPT_RL; ++i) { pg8::Unit pu; const bool ok = S.next(i, pu); pr[i] = (ok && t8 < pu.nv) ? LIST[pu.e * T + pu.mt * 256 + t8] >> 2 : 0;
;                   pv[i] = ok ? b_gu[(size_t)pu.e * 4096 + (t8 >> 7) * 2048 + pu.pn * 128 + (t8 & 127)] : 0.f; }
.LBB0_958:
	v_cmp_lt_i32_sdwa s[10:11], v0, s2 src0_sel:BYTE_0 src1_sel:DWORD
	s_and_b64 s[14:15], s[8:9], s[10:11]
	v_mov_b32_e32 v30, 0
	v_mov_b32_e32 v29, 0
	s_and_saveexec_b64 s[10:11], s[14:15]
	s_cbranch_execz .LBB0_960
	s_lshl_b32 s5, s4, 14
	s_lshl_b32 s13, s12, 8
	s_add_i32 s5, s5, s13
	v_or_b32_sdwa v32, s5, v0 dst_sel:DWORD dst_unused:UNUSED_PAD src0_sel:DWORD src1_sel:BYTE_0
	v_ashrrev_i32_e32 v33, 31, v32
	v_lshl_add_u64 v[32:33], v[32:33], 2, s[24:25]
	global_load_dword v29, v[32:33], off
.LBB0_960:
	s_or_b64 exec, exec, s[10:11]
	s_andn2_b64 vcc, exec, s[8:9]
	s_cbranch_vccnz .LBB0_962
	s_ashr_i32 s5, s4, 31
	s_lshl_b32 s8, s3, 7
	s_lshl_b64 s[10:11], s[4:5], 14
	s_ashr_i32 s9, s8, 31
	v_lshl_add_u64 v[30:31], v[6:7], 0, s[10:11]
	v_lshl_add_u64 v[30:31], s[8:9], 2, v[30:31]
	v_mov_b32_e32 v5, 0
	v_lshl_add_u64 v[30:31], v[30:31], 0, v[4:5]
	global_load_dword v30, v[30:31], off

; __global__ void __launch_bounds__(NTHREADS, 2) fwd(Args args) {
;     ...
;             { int pr[EPT_RL]; float pv[EPT_RL]; const int t8 = tid & 255;
; #pragma unroll
;               for (int i = 0; i < EPT_RL; ++i) { pg8::Unit pu; const bool ok = S.next(i, pu); pr[i] = (ok && t8 < pu.nv) ? LIST[pu.e * T + pu.mt * 256 + t8] >> 2 : 0;
;                   pv[i] = ok ? b_gu[(size_t)pu.e * 4096 + (t8 >> 7) * 2048 + pu.pn * 128 + (t8 & 127)] : 0.f; }
.LBB0_964:
	v_cmp_lt_i32_sdwa s[10:11], v0, s2 src0_sel:BYTE_0 src1_sel:DWORD
	s_and_b64 s[14:15], s[8:9], s[10:11]
	v_mov_b32_e32 v32, 0
	v_mov_b32_e32 v31, 0
	s_and_saveexec_b64 s[10:11], s[14:15]
	s_cbranch_execz .LBB0_966
	s_lshl_b32 s5, s4, 14
	s_lshl_b32 s13, s12, 8
	s_add_i32 s5, s5, s13
	v_or_b32_sdwa v34, s5, v0 dst_sel:DWORD dst_unused:UNUSED_PAD src0_sel:DWORD src1_sel:BYTE_0
	v_ashrrev_i32_e32 v35, 31, v34
	v_lshl_add_u64 v[34:35], v[34:35], 2, s[24:25]
	global_load_dword v31, v[34:35], off
.LBB0_966:
	s_or_b64 exec, exec, s[10:11]
	s_andn2_b64 vcc, exec, s[8:9]
	s_cbranch_vccnz .LBB0_968
	s_ashr_i32 s5, s4, 31
	s_lshl_b32 s8, s3, 7
	s_lshl_b64 s[10:11], s[4:5], 14
	s_ashr_i32 s9, s8, 31
	v_lshl_add_u64 v[32:33], v[6:7], 0, s[10:11]
	v_lshl_add_u64 v[32:33], s[8:9], 2, v[32:33]
	v_mov_b32_e32 v5, 0
	v_lshl_add_u64 v[32:33], v[32:33], 0, v[4:5]
	global_load_dword v32, v[32:33], off

; __global__ void __launch_bounds__(NTHREADS, 2) fwd(Args args) {
;     ...
;             { int pr[EPT_RL]; float pv[EPT_RL]; const int t8 = tid & 255;
; #pragma unroll
;               for (int i = 0; i < EPT_RL; ++i) { pg8::Unit pu; const bool ok = S.next(i, pu); pr[i] = (ok && t8 < pu.nv) ? LIST[pu.e * T + pu.mt * 256 + t8] >> 2 : 0;
;                   pv[i] = ok ? b_gu[(size_t)pu.e * 4096 + (t8 >> 7) * 2048 + pu.pn * 128 + (t8 & 127)] : 0.f; }
.LBB0_970:
	v_cmp_lt_i32_sdwa s[10:11], v0, s2 src0_sel:BYTE_0 src1_sel:DWORD
	s_and_b64 s[14:15], s[8:9], s[10:11]
	v_mov_b32_e32 v34, 0
	v_mov_b32_e32 v33, 0
	s_and_saveexec_b64 s[10:11], s[14:15]
	s_cbranch_execz .LBB0_972
	s_lshl_b32 s5, s4, 14
	s_lshl_b32 s13, s12, 8
	s_add_i32 s5, s5, s13
	v_or_b32_sdwa v36, s5, v0 dst_sel:DWORD dst_unused:UNUSED_PAD src0_sel:DWORD src1_sel:BYTE_0
	v_ashrrev_i32_e32 v37, 31, v36
	v_lshl_add_u64 v[36:37], v[36:37], 2, s[24:25]
	global_load_dword v33, v[36:37], off
.LBB0_972:
	s_or_b64 exec, exec, s[10:11]
	s_andn2_b64 vcc, exec, s[8:9]
	s_cbranch_vccnz .LBB0_974
	s_ashr_i32 s5, s4, 31
	s_lshl_b32 s8, s3, 7
	s_lshl_b64 s[10:11], s[4:5], 14
	s_ashr_i32 s9, s8, 31
	v_lshl_add_u64 v[34:35], v[6:7], 0, s[10:11]
	v_lshl_add_u64 v[34:35], s[8:9], 2, v[34:35]
	v_mov_b32_e32 v5, 0
	v_lshl_add_u64 v[34:35], v[34:35], 0, v[4:5]
	global_load_dword v34, v[34:35], off

; __global__ void __launch_bounds__(NTHREADS, 2) fwd(Args args) {
;     ...
;             { int pr[EPT_RL]; float pv[EPT_RL]; const int t8 = tid & 255;
; #pragma unroll
;               for (int i = 0; i < EPT_RL; ++i) { pg8::Unit pu; const bool ok = S.next(i, pu); pr[i] = (ok && t8 < pu.nv) ? LIST[pu.e * T + pu.mt * 256 + t8] >> 2 : 0;
;                   pv[i] = ok ? b_gu[(size_t)pu.e * 4096 + (t8 >> 7) * 2048 + pu.pn * 128 + (t8 & 127)] : 0.f; }
.LBB0_976:
	v_cmp_lt_i32_sdwa s[10:11], v0, s2 src0_sel:BYTE_0 src1_sel:DWORD
	s_and_b64 s[14:15], s[8:9], s[10:11]
	v_mov_b32_e32 v36, 0
	v_mov_b32_e32 v35, 0
	s_and_saveexec_b64 s[10:11], s[14:15]
	s_cbranch_execz .LBB0_978
	s_lshl_b32 s5, s4, 14
	s_lshl_b32 s13, s12, 8
	s_add_i32 s5, s5, s13
	v_or_b32_sdwa v38, s5, v0 dst_sel:DWORD dst_unused:UNUSED_PAD src0_sel:DWORD src1_sel:BYTE_0
	v_ashrrev_i32_e32 v39, 31, v38
	v_lshl_add_u64 v[38:39], v[38:39], 2, s[24:25]
	global_load_dword v35, v[38:39], off
.LBB0_978:
	s_or_b64 exec, exec, s[10:11]
	s_andn2_b64 vcc, exec, s[8:9]
	s_cbranch_vccnz .LBB0_980
	s_ashr_i32 s5, s4, 31
	s_lshl_b32 s8, s3, 7
	s_lshl_b64 s[10:11], s[4:5], 14
	s_ashr_i32 s9, s8, 31
	v_lshl_add_u64 v[36:37], v[6:7], 0, s[10:11]
	v_lshl_add_u64 v[36:37], s[8:9], 2, v[36:37]
	v_mov_b32_e32 v5, 0
	v_lshl_add_u64 v[36:37], v[36:37], 0, v[4:5]
	global_load_dword v36, v[36:37], off

; __global__ void __launch_bounds__(NTHREADS, 2) fwd(Args args) {
;     ...
;             { int pr[EPT_RL]; float pv[EPT_RL]; const int t8 = tid & 255;
; #pragma unroll
;               for (int i = 0; i < EPT_RL; ++i) { pg8::Unit pu; const bool ok = S.next(i, pu); pr[i] = (ok && t8 < pu.nv) ? LIST[pu.e * T + pu.mt * 256 + t8] >> 2 : 0;
;                   pv[i] = ok ? b_gu[(size_t)pu.e * 4096 + (t8 >> 7) * 2048 + pu.pn * 128 + (t8 & 127)] : 0.f; }
.LBB0_982:
	v_cmp_lt_i32_sdwa s[10:11], v0, s2 src0_sel:BYTE_0 src1_sel:DWORD
	s_and_b64 s[14:15], s[8:9], s[10:11]
	v_mov_b32_e32 v38, 0
	v_mov_b32_e32 v37, 0
	s_and_saveexec_b64 s[10:11], s[14:15]
	s_cbranch_execz .LBB0_984
	s_lshl_b32 s5, s4, 14
	s_lshl_b32 s13, s12, 8
	s_add_i32 s5, s5, s13
	v_or_b32_sdwa v40, s5, v0 dst_sel:DWORD dst_unused:UNUSED_PAD src0_sel:DWORD src1_sel:BYTE_0
	v_ashrrev_i32_e32 v41, 31, v40
	v_lshl_add_u64 v[40:41], v[40:41], 2, s[24:25]
	global_load_dword v37, v[40:41], off
.LBB0_984:
	s_or_b64 exec, exec, s[10:11]
	s_andn2_b64 vcc, exec, s[8:9]
	s_cbranch_vccnz .LBB0_986
	s_ashr_i32 s5, s4, 31
	s_lshl_b32 s8, s3, 7
	s_lshl_b64 s[10:11], s[4:5], 14
	s_ashr_i32 s9, s8, 31
	v_lshl_add_u64 v[38:39], v[6:7], 0, s[10:11]
	v_lshl_add_u64 v[38:39], s[8:9], 2, v[38:39]
	v_mov_b32_e32 v5, 0
	v_lshl_add_u64 v[38:39], v[38:39], 0, v[4:5]
	global_load_dword v38, v[38:39], off

; __global__ void __launch_bounds__(NTHREADS, 2) fwd(Args args) {
;     ...
;             { int pr[EPT_RL]; float pv[EPT_RL]; const int t8 = tid & 255;
; #pragma unroll
;               for (int i = 0; i < EPT_RL; ++i) { pg8::Unit pu; const bool ok = S.next(i, pu); pr[i] = (ok && t8 < pu.nv) ? LIST[pu.e * T + pu.mt * 256 + t8] >> 2 : 0;
;                   pv[i] = ok ? b_gu[(size_t)pu.e * 4096 + (t8 >> 7) * 2048 + pu.pn * 128 + (t8 & 127)] : 0.f; }
.LBB0_988:
	v_cmp_lt_i32_sdwa s[10:11], v0, s2 src0_sel:BYTE_0 src1_sel:DWORD
	s_and_b64 s[14:15], s[8:9], s[10:11]
	v_mov_b32_e32 v40, 0
	v_mov_b32_e32 v39, 0
	s_and_saveexec_b64 s[10:11], s[14:15]
	s_cbranch_execz .LBB0_990
	s_lshl_b32 s5, s4, 14
	s_lshl_b32 s13, s12, 8
	s_add_i32 s5, s5, s13
	v_or_b32_sdwa v42, s5, v0 dst_sel:DWORD dst_unused:UNUSED_PAD src0_sel:DWORD src1_sel:BYTE_0
	v_ashrrev_i32_e32 v43, 31, v42
	v_lshl_add_u64 v[42:43], v[42:43], 2, s[24:25]
	global_load_dword v39, v[42:43], off
.LBB0_990:
	s_or_b64 exec, exec, s[10:11]
	s_andn2_b64 vcc, exec, s[8:9]
	s_cbranch_vccnz .LBB0_992
	s_ashr_i32 s5, s4, 31
	s_lshl_b32 s8, s3, 7
	s_lshl_b64 s[10:11], s[4:5], 14
	s_ashr_i32 s9, s8, 31
	v_lshl_add_u64 v[40:41], v[6:7], 0, s[10:11]
	v_lshl_add_u64 v[40:41], s[8:9], 2, v[40:41]
	v_mov_b32_e32 v5, 0
	v_lshl_add_u64 v[40:41], v[40:41], 0, v[4:5]
	global_load_dword v40, v[40:41], off

; __global__ void __launch_bounds__(NTHREADS, 2) fwd(Args args) {
;     ...
;             { int pr[EPT_RL]; float pv[EPT_RL]; const int t8 = tid & 255;
; #pragma unroll
;               for (int i = 0; i < EPT_RL; ++i) { pg8::Unit pu; const bool ok = S.next(i, pu); pr[i] = (ok && t8 < pu.nv) ? LIST[pu.e * T + pu.mt * 256 + t8] >> 2 : 0;
;                   pv[i] = ok ? b_gu[(size_t)pu.e * 4096 + (t8 >> 7) * 2048 + pu.pn * 128 + (t8 & 127)] : 0.f; }
.LBB0_994:
	v_cmp_lt_i32_sdwa s[10:11], v0, s2 src0_sel:BYTE_0 src1_sel:DWORD
	s_and_b64 s[14:15], s[8:9], s[10:11]
	v_mov_b32_e32 v42, 0
	v_mov_b32_e32 v41, 0
	s_and_saveexec_b64 s[10:11], s[14:15]
	s_cbranch_execz .LBB0_996
	s_lshl_b32 s5, s4, 14
	s_lshl_b32 s13, s12, 8
	s_add_i32 s5, s5, s13
	v_or_b32_sdwa v44, s5, v0 dst_sel:DWORD dst_unused:UNUSED_PAD src0_sel:DWORD src1_sel:BYTE_0
	v_ashrrev_i32_e32 v45, 31, v44
	v_lshl_add_u64 v[44:45], v[44:45], 2, s[24:25]
	global_load_dword v41, v[44:45], off
.LBB0_996:
	s_or_b64 exec, exec, s[10:11]
	s_andn2_b64 vcc, exec, s[8:9]
	s_cbranch_vccnz .LBB0_998
	s_ashr_i32 s5, s4, 31
	s_lshl_b32 s8, s3, 7
	s_lshl_b64 s[10:11], s[4:5], 14
	s_ashr_i32 s9, s8, 31
	v_lshl_add_u64 v[42:43], v[6:7], 0, s[10:11]
	v_lshl_add_u64 v[42:43], s[8:9], 2, v[42:43]
	v_mov_b32_e32 v5, 0
	v_lshl_add_u64 v[42:43], v[42:43], 0, v[4:5]
	global_load_dword v42, v[42:43], off

; __global__ void __launch_bounds__(NTHREADS, 2) fwd(Args args) {
;     ...
;             { int pr[EPT_RL]; float pv[EPT_RL]; const int t8 = tid & 255;
; #pragma unroll
;               for (int i = 0; i < EPT_RL; ++i) { pg8::Unit pu; const bool ok = S.next(i, pu); pr[i] = (ok && t8 < pu.nv) ? LIST[pu.e * T + pu.mt * 256 + t8] >> 2 : 0;
;                   pv[i] = ok ? b_gu[(size_t)pu.e * 4096 + (t8 >> 7) * 2048 + pu.pn * 128 + (t8 & 127)] : 0.f; }
.LBB0_1000:
	v_cmp_lt_i32_sdwa s[10:11], v0, s2 src0_sel:BYTE_0 src1_sel:DWORD
	s_and_b64 s[14:15], s[8:9], s[10:11]
	v_mov_b32_e32 v44, 0
	v_mov_b32_e32 v43, 0
	s_and_saveexec_b64 s[10:11], s[14:15]
	s_cbranch_execz .LBB0_1002
	s_lshl_b32 s5, s4, 14
	s_lshl_b32 s13, s12, 8
	s_add_i32 s5, s5, s13
	v_or_b32_sdwa v46, s5, v0 dst_sel:DWORD dst_unused:UNUSED_PAD src0_sel:DWORD src1_sel:BYTE_0
	v_ashrrev_i32_e32 v47, 31, v46
	v_lshl_add_u64 v[46:47], v[46:47], 2, s[24:25]
	global_load_dword v43, v[46:47], off
.LBB0_1002:
	s_or_b64 exec, exec, s[10:11]
	s_andn2_b64 vcc, exec, s[8:9]
	s_cbranch_vccnz .LBB0_1004
	s_ashr_i32 s5, s4, 31
	s_lshl_b32 s8, s3, 7
	s_lshl_b64 s[10:11], s[4:5], 14
	s_ashr_i32 s9, s8, 31
	v_lshl_add_u64 v[44:45], v[6:7], 0, s[10:11]
	v_lshl_add_u64 v[44:45], s[8:9], 2, v[44:45]
	v_mov_b32_e32 v5, 0
	v_lshl_add_u64 v[44:45], v[44:45], 0, v[4:5]
	global_load_dword v44, v[44:45], off

; __global__ void __launch_bounds__(NTHREADS, 2) fwd(Args args) {
;     ...
;             { int pr[EPT_RL]; float pv[EPT_RL]; const int t8 = tid & 255;
; #pragma unroll
;               for (int i = 0; i < EPT_RL; ++i) { pg8::Unit pu; const bool ok = S.next(i, pu); pr[i] = (ok && t8 < pu.nv) ? LIST[pu.e * T + pu.mt * 256 + t8] >> 2 : 0;
;                   pv[i] = ok ? b_gu[(size_t)pu.e * 4096 + (t8 >> 7) * 2048 + pu.pn * 128 + (t8 & 127)] : 0.f; }
.LBB0_1006:
	v_cmp_lt_i32_sdwa s[10:11], v0, s2 src0_sel:BYTE_0 src1_sel:DWORD
	s_and_b64 s[14:15], s[8:9], s[10:11]
	v_mov_b32_e32 v46, 0
	v_mov_b32_e32 v45, 0
	s_and_saveexec_b64 s[10:11], s[14:15]
	s_cbranch_execz .LBB0_1008
	s_lshl_b32 s5, s4, 14
	s_lshl_b32 s13, s12, 8
	s_add_i32 s5, s5, s13
	v_or_b32_sdwa v48, s5, v0 dst_sel:DWORD dst_unused:UNUSED_PAD src0_sel:DWORD src1_sel:BYTE_0
	v_ashrrev_i32_e32 v49, 31, v48
	v_lshl_add_u64 v[48:49], v[48:49], 2, s[24:25]
	global_load_dword v45, v[48:49], off
.LBB0_1008:
	s_or_b64 exec, exec, s[10:11]
	s_andn2_b64 vcc, exec, s[8:9]
	s_cbranch_vccnz .LBB0_1010
	s_ashr_i32 s5, s4, 31
	s_lshl_b32 s8, s3, 7
	s_lshl_b64 s[10:11], s[4:5], 14
	s_ashr_i32 s9, s8, 31
	v_lshl_add_u64 v[46:47], v[6:7], 0, s[10:11]
	v_lshl_add_u64 v[46:47], s[8:9], 2, v[46:47]
	v_mov_b32_e32 v5, 0
	v_lshl_add_u64 v[46:47], v[46:47], 0, v[4:5]
	global_load_dword v46, v[46:47], off

; #define LBAR() do { asm volatile("s_waitcnt lgkmcnt(0)" ::: "memory"); __builtin_amdgcn_s_barrier(); asm volatile("" ::: "memory"); } while (0)
; __device__ __forceinline__ unsigned f2bf(float f) { return pk2(f, 0.f) & 0xffffu; }
; __global__ void __launch_bounds__(NTHREADS, 2) fwd(Args args) {
;     ...
;             { int pr[EPT_RL]; float pv[EPT_RL]; const int t8 = tid & 255;
; #pragma unroll
;               for (int i = 0; i < EPT_RL; ++i) { pg8::Unit pu; const bool ok = S.next(i, pu); pr[i] = (ok && t8 < pu.nv) ? LIST[pu.e * T + pu.mt * 256 + t8] >> 2 : 0;
;                   pv[i] = ok ? b_gu[(size_t)pu.e * 4096 + (t8 >> 7) * 2048 + pu.pn * 128 + (t8 & 127)] : 0.f; }
; #pragma unroll
;               for (int i = 0; i < EPT_RL; ++i) if (tid < 256) { RL[i * 256 + tid] = (unsigned short)pr[i]; BT[i * 256 + tid] = (bf16)f2bf(pv[i]); } }
;             LBAR();
.LBB0_1014:
	s_or_b64 exec, exec, s[10:11]
	s_andn2_b64 vcc, exec, s[8:9]
	s_cbranch_vccnz .LBB0_1016
	s_ashr_i32 s5, s4, 31
	s_lshl_b32 s2, s3, 7
	s_lshl_b64 s[4:5], s[4:5], 14
	s_ashr_i32 s3, s2, 31
	v_lshl_add_u64 v[6:7], v[6:7], 0, s[4:5]
	v_lshl_add_u64 v[6:7], s[2:3], 2, v[6:7]
	v_mov_b32_e32 v5, 0
	v_lshl_add_u64 v[4:5], v[6:7], 0, v[4:5]
	global_load_dword v5, v[4:5], off
.LBB0_1016:
	s_waitcnt vmcnt(0)
	v_lshrrev_b32_e32 v9, 2, v9
	v_cvt_pk_bf16_f32 v3, v3, s0
	v_lshrrev_b32_e32 v2, 2, v2
	v_cvt_pk_bf16_f32 v10, v10, s0
	v_lshrrev_b32_e32 v11, 2, v11
	v_cvt_pk_bf16_f32 v12, v12, s0
	v_lshrrev_b32_e32 v13, 2, v13
	v_cvt_pk_bf16_f32 v14, v14, s0
	v_lshrrev_b32_e32 v15, 2, v15
	v_cvt_pk_bf16_f32 v16, v16, s0
	v_lshrrev_b32_e32 v17, 2, v17
	v_cvt_pk_bf16_f32 v18, v18, s0
	v_lshrrev_b32_e32 v19, 2, v19
	v_cvt_pk_bf16_f32 v20, v20, s0
	v_lshrrev_b32_e32 v21, 2, v21
	v_cvt_pk_bf16_f32 v22, v22, s0
	v_lshrrev_b32_e32 v23, 2, v23
	v_cvt_pk_bf16_f32 v24, v24, s0
	v_lshrrev_b32_e32 v25, 2, v25
	v_cvt_pk_bf16_f32 v26, v26, s0
	v_lshrrev_b32_e32 v27, 2, v27
	v_cvt_pk_bf16_f32 v28, v28, s0
	v_lshrrev_b32_e32 v29, 2, v29
	v_cvt_pk_bf16_f32 v30, v30, s0
	v_lshrrev_b32_e32 v31, 2, v31
	v_cvt_pk_bf16_f32 v32, v32, s0
	v_lshrrev_b32_e32 v33, 2, v33
	v_cvt_pk_bf16_f32 v34, v34, s0
	v_lshrrev_b32_e32 v35, 2, v35
	v_cvt_pk_bf16_f32 v36, v36, s0
	v_lshrrev_b32_e32 v37, 2, v37
	v_cvt_pk_bf16_f32 v38, v38, s0
	v_lshrrev_b32_e32 v39, 2, v39
	v_cvt_pk_bf16_f32 v40, v40, s0
	v_lshrrev_b32_e32 v41, 2, v41
	v_cvt_pk_bf16_f32 v42, v42, s0
	v_lshrrev_b32_e32 v43, 2, v43
	v_cvt_pk_bf16_f32 v44, v44, s0
	v_lshrrev_b32_e32 v45, 2, v45
	v_cvt_pk_bf16_f32 v46, v46, s0
	v_lshrrev_b32_e32 v47, 2, v47
	v_cvt_pk_bf16_f32 v5, v5, s0
	s_movk_i32 s2, 0x100
	v_cmp_gt_u32_e32 vcc, s2, v0
	s_and_saveexec_b64 s[4:5], vcc
	s_cbranch_execz .LBB0_1018
	v_lshlrev_b32_e32 v4, 1, v0
	s_add_i32 s2, 0, 0x24200
	v_add_u32_e32 v6, s2, v4
	s_add_i32 s3, 0, 0x21800
	ds_write_b16 v6, v9
	v_add_u32_e32 v6, s3, v4
	ds_write_b16 v6, v3
	v_or_b32_e32 v3, 0x200, v4
	v_add_u32_e32 v6, s2, v3
	ds_write_b16 v6, v2
	v_add_u32_e32 v2, s3, v3
	ds_write_b16 v2, v10
	v_or_b32_e32 v2, 0x400, v4
	v_add_u32_e32 v3, s2, v2
	v_add_u32_e32 v2, s3, v2
	ds_write_b16 v2, v12
	v_or_b32_e32 v2, 0x600, v4
	ds_write_b16 v3, v11
	v_add_u32_e32 v3, s2, v2
	v_add_u32_e32 v2, s3, v2
	ds_write_b16 v2, v14
	v_or_b32_e32 v2, 0x800, v4
	ds_write_b16 v3, v13
	v_add_u32_e32 v3, s2, v2
	v_add_u32_e32 v2, s3, v2
	ds_write_b16 v2, v16
	v_or_b32_e32 v2, 0xa00, v4
	ds_write_b16 v3, v15
	v_add_u32_e32 v3, s2, v2
	v_add_u32_e32 v2, s3, v2
	ds_write_b16 v2, v18
	v_or_b32_e32 v2, 0xc00, v4
	ds_write_b16 v3, v17
	v_add_u32_e32 v3, s2, v2
	v_add_u32_e32 v2, s3, v2
	ds_write_b16 v2, v20
	v_or_b32_e32 v2, 0xe00, v4
	ds_write_b16 v3, v19
	v_add_u32_e32 v3, s2, v2
	v_add_u32_e32 v2, s3, v2
	ds_write_b16 v2, v22
	v_or_b32_e32 v2, 0x1000, v4
	ds_write_b16 v3, v21
	v_add_u32_e32 v3, s2, v2
	v_add_u32_e32 v2, s3, v2
	ds_write_b16 v2, v24
	v_or_b32_e32 v2, 0x1200, v4
	ds_write_b16 v3, v23
	v_add_u32_e32 v3, s2, v2
	v_add_u32_e32 v2, s3, v2
	ds_write_b16 v2, v26
	v_or_b32_e32 v2, 0x1400, v4
	ds_write_b16 v3, v25
	v_add_u32_e32 v3, s2, v2
	v_add_u32_e32 v2, s3, v2
	ds_write_b16 v2, v28
	v_or_b32_e32 v2, 0x1600, v4
	ds_write_b16 v3, v27
	v_add_u32_e32 v3, s2, v2
	v_add_u32_e32 v2, s3, v2
	ds_write_b16 v2, v30
	v_or_b32_e32 v2, 0x1800, v4
	ds_write_b16 v3, v29
	v_add_u32_e32 v3, s2, v2
	v_add_u32_e32 v2, s3, v2
	ds_write_b16 v2, v32
	v_or_b32_e32 v2, 0x1a00, v4
	ds_write_b16 v3, v31
	v_add_u32_e32 v3, s2, v2
	v_add_u32_e32 v2, s3, v2
	ds_write_b16 v2, v34
	v_or_b32_e32 v2, 0x1c00, v4
	ds_write_b16 v3, v33
	v_add_u32_e32 v3, s2, v2
	v_add_u32_e32 v2, s3, v2
	ds_write_b16 v2, v36
	v_or_b32_e32 v2, 0x1e00, v4
	ds_write_b16 v3, v35
	v_add_u32_e32 v3, s2, v2
	v_add_u32_e32 v2, s3, v2
	ds_write_b16 v2, v38
	v_or_b32_e32 v2, 0x2000, v4
	ds_write_b16 v3, v37
	v_add_u32_e32 v3, s2, v2
	v_add_u32_e32 v2, s3, v2
	ds_write_b16 v2, v40
	v_or_b32_e32 v2, 0x2200, v4
	ds_write_b16 v3, v39
	v_add_u32_e32 v3, s2, v2
	v_add_u32_e32 v2, s3, v2
	ds_write_b16 v2, v42
	v_or_b32_e32 v2, 0x2400, v4
	ds_write_b16 v3, v41
	v_add_u32_e32 v3, s2, v2
	v_add_u32_e32 v2, s3, v2
	ds_write_b16 v2, v44
	v_or_b32_e32 v2, 0x2600, v4
	ds_write_b16 v3, v43
	v_add_u32_e32 v3, s2, v2
	v_add_u32_e32 v2, s3, v2
	ds_write_b16 v2, v46
	v_or_b32_e32 v2, 0x2800, v4
	ds_write_b16 v3, v45
	v_add_u32_e32 v3, s2, v2
	v_add_u32_e32 v2, s3, v2
	ds_write_b16 v3, v47
	ds_write_b16 v2, v5
.LBB0_1018:
	s_or_b64 exec, exec, s[4:5]
	v_readlane_b32 s10, v1, 0
	s_waitcnt lgkmcnt(0)
	s_barrier
	s_cmp_gt_i32 s10, -1
	s_cselect_b64 s[4:5], -1, 0
	v_readfirstlane_b32 s9, v0
	s_and_b64 vcc, exec, s[4:5]
	s_cbranch_vccz .LBB0_1020
	v_readlane_b32 s8, v195, 0
	s_andn2_b64 vcc, exec, s[4:5]
	s_cbranch_vccz .LBB0_1021
	s_branch .LBB0_1052
	s_nop 0
	s_nop 0
	s_nop 0
	s_nop 0
	s_nop 0
	s_nop 0
	s_nop 0
	s_nop 0
	s_nop 0
	s_nop 0
	s_nop 0
	s_nop 0
	s_nop 0
	s_nop 0
	s_nop 0
	s_nop 0
	s_nop 0
	s_nop 0
	s_nop 0
	s_nop 0
	s_nop 0
	s_nop 0
	s_nop 0
	s_nop 0
	s_nop 0
	s_nop 0
	s_nop 0
	s_nop 0
	s_nop 0
	s_nop 0
	s_nop 0
	s_nop 0
	s_nop 0
	s_nop 0
	s_nop 0
	s_nop 0
	s_nop 0
	s_nop 0
	s_nop 0
	s_nop 0
	s_nop 0
